# loader issues B-fragment reads before the z16 conversion; output wave waits lgkmcnt(1) before first MFMAs; loop increments moved before the barrier wait
# baseline (speedup 1.0000x reference)
.LBB0_82:
	ds_read_b128 v[194:197], v193
	ds_read_b128 v[198:201], v193 offset:32
	ds_read_b128 v[202:205], v193 offset:64
	ds_read_b128 v[206:209], v193 offset:96
	s_waitcnt vmcnt(3)
	v_cvt_pk_f16_f32 v67, v168, v169
	v_cvt_pk_f16_f32 v66, v166, v167
	ds_write_b64 v192, v[66:67]
	s_waitcnt vmcnt(2)
	v_cvt_pk_f16_f32 v67, v164, v165
	v_cvt_pk_f16_f32 v66, v162, v163
	ds_write_b64 v192, v[66:67] offset:2304
	s_add_i32 s6, s0, -1
	s_add_i32 s5, s0, -2
	s_and_b32 s6, s6, 3
	s_min_u32 s7, s5, 12
	s_lshl_b32 s6, s6, 13
	v_lshl_add_u32 v66, s7, 13, v190
	s_add_i32 s6, s6, 0x12000
	v_or_b32_e32 v66, v66, v178
	v_lshl_or_b32 v67, v187, 4, s6
	v_lshl_or_b32 v84, v188, 4, s6
	v_or_b32_e32 v85, 0x1000, v66
	ds_write_b128 v67, v[166:169]
	ds_write_b128 v84, v[162:165]
	global_load_dwordx4 v[166:169], v66, s[20:21] nt
	global_load_dwordx4 v[162:165], v85, s[20:21] nt
	s_cmp_gt_u32 s5, 13
	s_waitcnt lgkmcnt(7)
	v_mfma_f32_32x32x16_f16 v[66:81], v[98:101], v[194:197], v[2:17]
	s_waitcnt lgkmcnt(6)
	v_mfma_f32_32x32x16_f16 v[66:81], v[102:105], v[198:201], v[66:81]
	s_waitcnt lgkmcnt(5)
	v_mfma_f32_32x32x16_f16 v[66:81], v[106:109], v[202:205], v[66:81]
	s_waitcnt lgkmcnt(4)
	v_mfma_f32_32x32x16_f16 v[66:81], v[110:113], v[206:209], v[66:81]
	v_mfma_f32_32x32x16_f16 v[82:97], v[114:117], v[194:197], v[18:33]
	s_nop 10
	v_and_b32_e32 v66, 0xffffffc0, v66
	v_and_or_b32 v67, v67, s1, 1
	v_and_or_b32 v68, v68, s1, 2
	v_and_or_b32 v69, v69, s1, 3
	v_med3_f32 v211, v66, v67, s4
	v_and_or_b32 v70, v70, s1, 4
	v_min3_f32 v210, v66, s4, v67
	v_and_or_b32 v71, v71, s1, 5
	v_mfma_f32_32x32x16_f16 v[82:97], v[118:121], v[198:201], v[82:97]
	v_med3_f32 v214, v210, v68, v69
	v_and_or_b32 v72, v72, s1, 6
	v_min3_f32 v212, v210, v68, v69
	v_and_or_b32 v73, v73, s1, 7
	v_min3_f32 v213, v211, s4, v214
	v_med3_f32 v211, v212, v70, v71
	v_and_or_b32 v74, v74, s1, 8
	v_min3_f32 v210, v212, v70, v71
	v_mfma_f32_32x32x16_f16 v[82:97], v[122:125], v[202:205], v[82:97]
	v_and_or_b32 v75, v75, s1, 9
	v_med3_f32 v214, v210, v72, v73
	v_and_or_b32 v76, v76, s1, 10
	v_min3_f32 v212, v210, v72, v73
	v_and_or_b32 v77, v77, s1, 11
	v_min3_f32 v213, v213, v211, v214
	v_med3_f32 v211, v212, v74, v75
	v_and_or_b32 v78, v78, s1, 12
	v_mfma_f32_32x32x16_f16 v[82:97], v[126:129], v[206:209], v[82:97]
	v_min3_f32 v210, v212, v74, v75
	v_and_or_b32 v79, v79, s1, 13
	v_med3_f32 v214, v210, v76, v77
	v_and_or_b32 v80, v80, s1, 14
	v_min3_f32 v212, v210, v76, v77
	v_and_or_b32 v81, v81, s1, 15
	v_min3_f32 v213, v213, v211, v214
	v_med3_f32 v211, v212, v78, v79
	v_min3_f32 v210, v212, v78, v79
	v_med3_f32 v214, v210, v80, v81
	v_min3_f32 v212, v210, v80, v81
	v_min3_f32 v213, v213, v211, v214
	v_mfma_f32_32x32x16_f16 v[66:81], v[130:133], v[194:197], v[34:49]
	v_and_or_b32 v82, v82, s1, 16
	v_and_or_b32 v83, v83, s1, 17
	v_and_or_b32 v84, v84, s1, 18
	v_and_or_b32 v85, v85, s1, 19
	v_med3_f32 v211, v212, v82, v83
	v_and_or_b32 v86, v86, s1, 20
	v_min3_f32 v210, v212, v82, v83
	v_and_or_b32 v87, v87, s1, 21
	v_mfma_f32_32x32x16_f16 v[66:81], v[134:137], v[198:201], v[66:81]
	v_med3_f32 v214, v210, v84, v85
	v_and_or_b32 v88, v88, s1, 22
	v_min3_f32 v212, v210, v84, v85
	v_and_or_b32 v89, v89, s1, 23
	v_min3_f32 v213, v213, v211, v214
	v_med3_f32 v211, v212, v86, v87
	v_and_or_b32 v90, v90, s1, 24
	v_min3_f32 v210, v212, v86, v87
	v_mfma_f32_32x32x16_f16 v[66:81], v[138:141], v[202:205], v[66:81]
	v_and_or_b32 v91, v91, s1, 25
	v_med3_f32 v214, v210, v88, v89
	v_and_or_b32 v92, v92, s1, 26
	v_min3_f32 v212, v210, v88, v89
	v_and_or_b32 v93, v93, s1, 27
	v_min3_f32 v213, v213, v211, v214
	v_med3_f32 v211, v212, v90, v91
	v_and_or_b32 v94, v94, s1, 28
	v_mfma_f32_32x32x16_f16 v[66:81], v[142:145], v[206:209], v[66:81]
	v_min3_f32 v210, v212, v90, v91
	v_and_or_b32 v95, v95, s1, 29
	v_med3_f32 v214, v210, v92, v93
	v_and_or_b32 v96, v96, s1, 30
	v_min3_f32 v212, v210, v92, v93
	v_and_or_b32 v97, v97, s1, 31
	v_min3_f32 v213, v213, v211, v214
	v_med3_f32 v211, v212, v94, v95
	v_min3_f32 v210, v212, v94, v95
	v_med3_f32 v214, v210, v96, v97
	v_min3_f32 v212, v210, v96, v97
	v_min3_f32 v213, v213, v211, v214
	v_mfma_f32_32x32x16_f16 v[82:97], v[146:149], v[194:197], v[50:65]
	v_and_or_b32 v66, v66, s1, 32
	v_and_or_b32 v67, v67, s1, 33
	v_and_or_b32 v68, v68, s1, 34
	v_and_or_b32 v69, v69, s1, 35
	v_med3_f32 v211, v212, v66, v67
	v_and_or_b32 v70, v70, s1, 36
	v_min3_f32 v210, v212, v66, v67
	v_and_or_b32 v71, v71, s1, 37
	v_mfma_f32_32x32x16_f16 v[82:97], v[150:153], v[198:201], v[82:97]
	v_med3_f32 v214, v210, v68, v69
	v_and_or_b32 v72, v72, s1, 38
	v_min3_f32 v212, v210, v68, v69
	v_and_or_b32 v73, v73, s1, 39
	v_min3_f32 v213, v213, v211, v214
	v_med3_f32 v211, v212, v70, v71
	v_and_or_b32 v74, v74, s1, 40
	v_min3_f32 v210, v212, v70, v71
	v_mfma_f32_32x32x16_f16 v[82:97], v[154:157], v[202:205], v[82:97]
	v_and_or_b32 v75, v75, s1, 41
	v_med3_f32 v214, v210, v72, v73
	v_and_or_b32 v76, v76, s1, 42
	v_min3_f32 v212, v210, v72, v73
	v_and_or_b32 v77, v77, s1, 43
	v_min3_f32 v213, v213, v211, v214
	v_med3_f32 v211, v212, v74, v75
	v_and_or_b32 v78, v78, s1, 44
	v_mfma_f32_32x32x16_f16 v[82:97], v[158:161], v[206:209], v[82:97]
	v_min3_f32 v210, v212, v74, v75
	v_and_or_b32 v79, v79, s1, 45
	v_med3_f32 v214, v210, v76, v77
	v_and_or_b32 v80, v80, s1, 46
	v_min3_f32 v212, v210, v76, v77
	v_and_or_b32 v81, v81, s1, 47
	v_min3_f32 v213, v213, v211, v214
	v_med3_f32 v211, v212, v78, v79
	v_min3_f32 v210, v212, v78, v79
	v_med3_f32 v214, v210, v80, v81
	v_min3_f32 v212, v210, v80, v81
	v_min3_f32 v213, v213, v211, v214
	v_and_or_b32 v82, v82, s1, 48
	v_and_or_b32 v83, v83, s1, 49
	v_and_or_b32 v84, v84, s1, 50
	v_and_or_b32 v85, v85, s1, 51
	v_med3_f32 v211, v212, v82, v83
	v_and_or_b32 v86, v86, s1, 52
	v_min3_f32 v210, v212, v82, v83
	v_and_or_b32 v87, v87, s1, 53
	v_med3_f32 v214, v210, v84, v85
	v_and_or_b32 v88, v88, s1, 54
	v_min3_f32 v212, v210, v84, v85
	v_and_or_b32 v89, v89, s1, 55
	v_min3_f32 v213, v213, v211, v214
	v_med3_f32 v211, v212, v86, v87
	v_and_or_b32 v90, v90, s1, 56
	v_min3_f32 v210, v212, v86, v87
	v_and_or_b32 v91, v91, s1, 57
	v_med3_f32 v214, v210, v88, v89
	v_and_or_b32 v92, v92, s1, 58
	v_min3_f32 v212, v210, v88, v89
	v_and_or_b32 v93, v93, s1, 59
	v_min3_f32 v213, v213, v211, v214
	v_med3_f32 v211, v212, v90, v91
	v_and_or_b32 v94, v94, s1, 60
	v_min3_f32 v210, v212, v90, v91
	v_and_or_b32 v95, v95, s1, 61
	v_med3_f32 v214, v210, v92, v93
	v_and_or_b32 v96, v96, s1, 62
	v_min3_f32 v212, v210, v92, v93
	v_or_b32_e32 v97, 63, v97
	v_min3_f32 v213, v213, v211, v214
	v_med3_f32 v211, v212, v94, v95
	v_min3_f32 v210, v212, v94, v95
	v_med3_f32 v214, v210, v96, v97
	v_min3_f32 v212, v210, v96, v97
	v_min3_f32 v213, v213, v211, v214
	ds_write_b64 v189, v[212:213]
	s_waitcnt lgkmcnt(0)
	s_barrier
	s_cbranch_scc1 .LBB0_81
	s_and_b32 s6, s0, 2
	s_waitcnt vmcnt(3)
	v_cvt_pk_f16_f32 v67, v176, v177
	v_cvt_pk_f16_f32 v66, v174, v175
	s_lshl_b32 s6, s6, 13
	ds_write_b64 v192, v[66:67] offset:4608
	s_waitcnt vmcnt(2)
	v_cvt_pk_f16_f32 v67, v172, v173
	v_cvt_pk_f16_f32 v66, v170, v171
	s_or_b32 s6, s6, 0x12000
	ds_write_b64 v192, v[66:67] offset:6912
	v_lshl_or_b32 v66, v187, 4, s6
	ds_write_b128 v66, v[174:177]
	v_lshl_or_b32 v66, v188, 4, s6
	ds_write_b128 v66, v[170:173]
	s_branch .LBB0_81

.LBB0_87:
	s_waitcnt lgkmcnt(0)
	s_barrier
	s_add_i32 s17, s17, 1
	s_cmp_lg_u32 s17, 16
	s_cbranch_scc0 .LBB0_97

.Low_m_done:
	s_or_b64 exec, exec, s[6:7]
	s_waitcnt lgkmcnt(1)
	v_mfma_f32_32x32x16_f16 v[66:81], v[98:101], v[194:197], v[2:17]
	v_mfma_f32_32x32x16_f16 v[66:81], v[102:105], v[198:201], v[66:81]
	v_add_u32_e32 v254, 0x20c00, v188
	s_waitcnt lgkmcnt(0)
	ds_read_b32 v191, v254 offset:64
	ds_read_b32 v192, v254
	v_mfma_f32_32x32x16_f16 v[66:81], v[106:109], v[202:205], v[66:81]
	v_mfma_f32_32x32x16_f16 v[66:81], v[110:113], v[206:209], v[66:81]
	v_mfma_f32_32x32x16_f16 v[82:97], v[114:117], v[194:197], v[18:33]
	s_waitcnt lgkmcnt(0)
	v_and_b32_e32 v212, s27, v191
	v_lshl_or_b32 v212, v212, 8, v178
	global_load_dwordx4 v[162:165], v212, s[22:23]
	v_and_b32_e32 v213, s27, v192
	v_lshl_or_b32 v213, v213, 8, v178
	global_load_dwordx4 v[246:249], v213, s[22:23]
	s_and_b32 s1, s29, 3
	v_lshl_add_u32 v212, s1, 13, v175
	v_lshl_add_u32 v213, s1, 13, v174
	ds_read_b128 v[224:227], v212
	ds_read_b128 v[228:231], v213
	v_and_b32_e32 v66, 0xffffffc0, v66
	v_and_or_b32 v67, v67, s16, 1
	v_and_or_b32 v68, v68, s16, 2
	v_and_or_b32 v69, v69, s16, 3
	v_med3_f32 v211, v66, v67, s25
	v_and_or_b32 v70, v70, s16, 4
	v_min3_f32 v210, v66, s25, v67
	v_and_or_b32 v71, v71, s16, 5
	v_mfma_f32_32x32x16_f16 v[82:97], v[118:121], v[198:201], v[82:97]
	v_med3_f32 v214, v210, v68, v69
	v_and_or_b32 v72, v72, s16, 6
	v_min3_f32 v212, v210, v68, v69
	v_and_or_b32 v73, v73, s16, 7
	v_min3_f32 v213, v211, s25, v214
	v_med3_f32 v211, v212, v70, v71
	v_and_or_b32 v74, v74, s16, 8
	v_min3_f32 v210, v212, v70, v71
	v_mfma_f32_32x32x16_f16 v[82:97], v[122:125], v[202:205], v[82:97]
	v_and_or_b32 v75, v75, s16, 9
	v_med3_f32 v214, v210, v72, v73
	v_and_or_b32 v76, v76, s16, 10
	v_min3_f32 v212, v210, v72, v73
	v_and_or_b32 v77, v77, s16, 11
	v_min3_f32 v213, v213, v211, v214
	v_med3_f32 v211, v212, v74, v75
	v_and_or_b32 v78, v78, s16, 12
	v_mfma_f32_32x32x16_f16 v[82:97], v[126:129], v[206:209], v[82:97]
	v_min3_f32 v210, v212, v74, v75
	v_and_or_b32 v79, v79, s16, 13
	v_med3_f32 v214, v210, v76, v77
	v_and_or_b32 v80, v80, s16, 14
	v_min3_f32 v212, v210, v76, v77
	v_and_or_b32 v81, v81, s16, 15
	v_min3_f32 v213, v213, v211, v214
	v_med3_f32 v211, v212, v78, v79
	v_min3_f32 v210, v212, v78, v79
	v_med3_f32 v214, v210, v80, v81
	v_min3_f32 v212, v210, v80, v81
	v_min3_f32 v213, v213, v211, v214
	v_mfma_f32_32x32x16_f16 v[66:81], v[130:133], v[194:197], v[34:49]
	v_and_or_b32 v82, v82, s16, 16
	v_and_or_b32 v83, v83, s16, 17
	v_and_or_b32 v84, v84, s16, 18
	v_and_or_b32 v85, v85, s16, 19
	v_med3_f32 v211, v212, v82, v83
	v_and_or_b32 v86, v86, s16, 20
	v_min3_f32 v210, v212, v82, v83
	v_and_or_b32 v87, v87, s16, 21
	v_mfma_f32_32x32x16_f16 v[66:81], v[134:137], v[198:201], v[66:81]
	v_med3_f32 v214, v210, v84, v85
	v_and_or_b32 v88, v88, s16, 22
	v_min3_f32 v212, v210, v84, v85
	v_and_or_b32 v89, v89, s16, 23
	v_min3_f32 v213, v213, v211, v214
	v_med3_f32 v211, v212, v86, v87
	v_and_or_b32 v90, v90, s16, 24
	v_min3_f32 v210, v212, v86, v87
	v_mfma_f32_32x32x16_f16 v[66:81], v[138:141], v[202:205], v[66:81]
	v_and_or_b32 v91, v91, s16, 25
	v_med3_f32 v214, v210, v88, v89
	v_and_or_b32 v92, v92, s16, 26
	v_min3_f32 v212, v210, v88, v89
	v_and_or_b32 v93, v93, s16, 27
	v_min3_f32 v213, v213, v211, v214
	v_med3_f32 v211, v212, v90, v91
	v_and_or_b32 v94, v94, s16, 28
	v_mfma_f32_32x32x16_f16 v[66:81], v[142:145], v[206:209], v[66:81]
	v_min3_f32 v210, v212, v90, v91
	v_and_or_b32 v95, v95, s16, 29
	v_med3_f32 v214, v210, v92, v93
	v_and_or_b32 v96, v96, s16, 30
	v_min3_f32 v212, v210, v92, v93
	v_and_or_b32 v97, v97, s16, 31
	v_min3_f32 v213, v213, v211, v214
	v_med3_f32 v211, v212, v94, v95
	v_min3_f32 v210, v212, v94, v95
	v_med3_f32 v214, v210, v96, v97
	v_min3_f32 v212, v210, v96, v97
	v_min3_f32 v213, v213, v211, v214
	v_mfma_f32_32x32x16_f16 v[82:97], v[146:149], v[194:197], v[50:65]
	v_and_or_b32 v66, v66, s16, 32
	v_and_or_b32 v67, v67, s16, 33
	v_and_or_b32 v68, v68, s16, 34
	v_and_or_b32 v69, v69, s16, 35
	v_med3_f32 v211, v212, v66, v67
	v_and_or_b32 v70, v70, s16, 36
	v_min3_f32 v210, v212, v66, v67
	v_and_or_b32 v71, v71, s16, 37
	v_mfma_f32_32x32x16_f16 v[82:97], v[150:153], v[198:201], v[82:97]
	v_med3_f32 v214, v210, v68, v69
	v_and_or_b32 v72, v72, s16, 38
	v_min3_f32 v212, v210, v68, v69
	v_and_or_b32 v73, v73, s16, 39
	v_min3_f32 v213, v213, v211, v214
	v_med3_f32 v211, v212, v70, v71
	v_and_or_b32 v74, v74, s16, 40
	v_min3_f32 v210, v212, v70, v71
	v_mfma_f32_32x32x16_f16 v[82:97], v[154:157], v[202:205], v[82:97]
	v_and_or_b32 v75, v75, s16, 41
	v_med3_f32 v214, v210, v72, v73
	v_and_or_b32 v76, v76, s16, 42
	v_min3_f32 v212, v210, v72, v73
	v_and_or_b32 v77, v77, s16, 43
	v_min3_f32 v213, v213, v211, v214
	v_med3_f32 v211, v212, v74, v75
	v_and_or_b32 v78, v78, s16, 44
	v_mfma_f32_32x32x16_f16 v[82:97], v[158:161], v[206:209], v[82:97]
	v_min3_f32 v210, v212, v74, v75
	v_and_or_b32 v79, v79, s16, 45
	v_med3_f32 v214, v210, v76, v77
	v_and_or_b32 v80, v80, s16, 46
	v_min3_f32 v212, v210, v76, v77
	v_and_or_b32 v81, v81, s16, 47
	v_min3_f32 v213, v213, v211, v214
	v_med3_f32 v211, v212, v78, v79
	v_min3_f32 v210, v212, v78, v79
	v_med3_f32 v214, v210, v80, v81
	v_min3_f32 v212, v210, v80, v81
	v_min3_f32 v213, v213, v211, v214
	v_and_or_b32 v82, v82, s16, 48
	v_and_or_b32 v83, v83, s16, 49
	v_and_or_b32 v84, v84, s16, 50
	v_and_or_b32 v85, v85, s16, 51
	v_med3_f32 v211, v212, v82, v83
	v_and_or_b32 v86, v86, s16, 52
	v_min3_f32 v210, v212, v82, v83
	v_and_or_b32 v87, v87, s16, 53
	v_med3_f32 v214, v210, v84, v85
	v_and_or_b32 v88, v88, s16, 54
	v_min3_f32 v212, v210, v84, v85
	v_and_or_b32 v89, v89, s16, 55
	v_min3_f32 v213, v213, v211, v214
	v_med3_f32 v211, v212, v86, v87
	v_and_or_b32 v90, v90, s16, 56
	v_min3_f32 v210, v212, v86, v87
	v_and_or_b32 v91, v91, s16, 57
	v_med3_f32 v214, v210, v88, v89
	v_and_or_b32 v92, v92, s16, 58
	v_min3_f32 v212, v210, v88, v89
	v_and_or_b32 v93, v93, s16, 59
	v_min3_f32 v213, v213, v211, v214
	v_med3_f32 v211, v212, v90, v91
	v_and_or_b32 v94, v94, s16, 60
	v_min3_f32 v210, v212, v90, v91
	v_and_or_b32 v95, v95, s16, 61
	v_med3_f32 v214, v210, v92, v93
	v_and_or_b32 v96, v96, s16, 62
	v_min3_f32 v212, v210, v92, v93
	v_or_b32_e32 v97, 63, v97
	v_min3_f32 v213, v213, v211, v214
	v_med3_f32 v211, v212, v94, v95
	v_min3_f32 v210, v212, v94, v95
	v_med3_f32 v214, v210, v96, v97
	v_min3_f32 v212, v210, v96, v97
	v_min3_f32 v213, v213, v211, v214
	s_and_b32 s0, s17, 1
	s_mulk_i32 s0, 0x1200
	v_add_u32_e32 v254, s0, v177
	ds_write_b64 v254, v[212:213]
	v_add_u32_e32 v179, 0x1200, v179
	v_add_u32_e32 v188, 0x80, v188
	v_add_u32_e32 v186, 0x80, v186
	v_add_u32_e32 v166, 32, v166
	s_branch .LBB0_87
